# MLA layer-0 peeled last key tile: PV with 5 V fragments in flight instead of 8 serial LDS round trips
# baseline (speedup 1.0000x reference)
.LBB0_1044:
	v_add_f32_e32 v6, v6, v6
	v_fmac_f32_e32 v6, v16, v2
	v_add_u32_e32 v2, v231, v179
	v_cvt_pk_bf16_f32 v84, v84, v86
	v_cvt_pk_bf16_f32 v85, v82, v85
	v_cvt_pk_bf16_f32 v86, v15, v83
	v_cvt_pk_bf16_f32 v87, v14, v17
	v_cvt_pk_bf16_f32 v14, v9, v12
	v_cvt_pk_bf16_f32 v15, v7, v10
	v_cvt_pk_bf16_f32 v16, v5, v8
	v_cvt_pk_bf16_f32 v17, v11, v13
	v_add_u32_e32 v82, 0x1000, v2
	v_add_u32_e32 v83, 0x2000, v2
	v_add_u32_e32 v88, 0x3000, v2
	ds_read2_b64 v[248:251], v2 offset1:2
	ds_read2_b64 v[252:255], v82 offset0:64 offset1:66
	ds_read2_b64 v[238:241], v83 offset0:128 offset1:130
	ds_read2_b64 v[146:149], v88 offset0:192 offset1:194
	ds_read2_b64 v[150:153], v2 offset0:4 offset1:6
	s_andn2_b64 vcc, exec, s[6:7]
	s_waitcnt lgkmcnt(4)
	v_mfma_f32_32x32x16_bf16 v[66:81], v[248:251], v[84:87], v[66:81]
	ds_read2_b64 v[248:251], v82 offset0:68 offset1:70
	s_waitcnt lgkmcnt(4)
	v_mfma_f32_32x32x16_bf16 v[50:65], v[252:255], v[84:87], v[50:65]
	ds_read2_b64 v[252:255], v83 offset0:132 offset1:134
	s_waitcnt lgkmcnt(4)
	v_mfma_f32_32x32x16_bf16 v[34:49], v[238:241], v[84:87], v[34:49]
	ds_read2_b64 v[238:241], v88 offset0:196 offset1:198
	s_waitcnt lgkmcnt(4)
	v_mfma_f32_32x32x16_bf16 v[18:33], v[146:149], v[84:87], v[18:33]
	s_waitcnt lgkmcnt(3)
	v_mfma_f32_32x32x16_bf16 v[66:81], v[150:153], v[14:17], v[66:81]
	s_waitcnt lgkmcnt(2)
	v_mfma_f32_32x32x16_bf16 v[50:65], v[248:251], v[14:17], v[50:65]
	s_waitcnt lgkmcnt(1)
	v_mfma_f32_32x32x16_bf16 v[34:49], v[252:255], v[14:17], v[34:49]
	s_waitcnt lgkmcnt(0)
	s_barrier
	v_mfma_f32_32x32x16_bf16 v[18:33], v[238:241], v[14:17], v[18:33]
	s_cbranch_vccnz .LBB0_1046
	s_nop 0
	ds_write2st64_b32 v232, v66, v67 offset1:1
	ds_write2st64_b32 v232, v68, v69 offset0:2 offset1:3
	ds_write2st64_b32 v232, v70, v71 offset0:4 offset1:5
	ds_write2st64_b32 v232, v72, v73 offset0:6 offset1:7
	ds_write2st64_b32 v232, v74, v75 offset0:8 offset1:9
	ds_write2st64_b32 v232, v76, v77 offset0:10 offset1:11
	ds_write2st64_b32 v232, v78, v79 offset0:12 offset1:13
	ds_write2st64_b32 v232, v80, v81 offset0:14 offset1:15
	ds_write2st64_b32 v232, v50, v51 offset0:16 offset1:17
	ds_write2st64_b32 v232, v52, v53 offset0:18 offset1:19
	ds_write2st64_b32 v232, v54, v55 offset0:20 offset1:21
	ds_write2st64_b32 v232, v56, v57 offset0:22 offset1:23
	ds_write2st64_b32 v232, v58, v59 offset0:24 offset1:25
	ds_write2st64_b32 v232, v60, v61 offset0:26 offset1:27
	ds_write2st64_b32 v232, v62, v63 offset0:28 offset1:29
	ds_write2st64_b32 v232, v64, v65 offset0:30 offset1:31
	ds_write2st64_b32 v232, v34, v35 offset0:32 offset1:33
	ds_write2st64_b32 v232, v36, v37 offset0:34 offset1:35
	ds_write2st64_b32 v232, v38, v39 offset0:36 offset1:37
	ds_write2st64_b32 v232, v40, v41 offset0:38 offset1:39
	ds_write2st64_b32 v232, v42, v43 offset0:40 offset1:41
	ds_write2st64_b32 v232, v44, v45 offset0:42 offset1:43
	ds_write2st64_b32 v232, v46, v47 offset0:44 offset1:45
	ds_write2st64_b32 v232, v48, v49 offset0:46 offset1:47
	ds_write2st64_b32 v232, v18, v19 offset0:48 offset1:49
	ds_write2st64_b32 v232, v20, v21 offset0:50 offset1:51
	ds_write2st64_b32 v232, v22, v23 offset0:52 offset1:53
	ds_write2st64_b32 v232, v24, v25 offset0:54 offset1:55
	ds_write2st64_b32 v232, v26, v27 offset0:56 offset1:57
	ds_write2st64_b32 v232, v28, v29 offset0:58 offset1:59
	ds_write2st64_b32 v232, v30, v31 offset0:60 offset1:61
	ds_write2st64_b32 v232, v32, v33 offset0:62 offset1:63
	ds_write2st64_b32 v232, v4, v6 offset0:64 offset1:65
